# v034 with the MLA -mhat splat moved from the MFMA segment to the softmax segment tail
# baseline (speedup 1.0000x reference)
; #define SBAR() __builtin_amdgcn_sched_barrier(0)
; #define PK4(P, BASE, OUT) do { u32x4 w = {cvtpk(P[BASE + 0], P[BASE + 1]), cvtpk(P[BASE + 2], P[BASE + 3]), cvtpk(P[BASE + 4], P[BASE + 5]), cvtpk(P[BASE + 6], P[BASE + 7])}; \
;     OUT = *reinterpret_cast<bf16x8*>(&w); } while (0)
; __device__ __forceinline__ void smax_tile(f32x16& p0, f32x16& p1, float& mhat, float& l_reg, f32x16 (&o)[4], float* al_l, const bool first, int r32, int hi,
;                                           bf16x8& pa0, bf16x8& pa1, bf16x8& pa2, bf16x8& pa3) {
;     ...
; #pragma unroll
;     for (int r = 0; r < 16; ++r) p0[r] = __builtin_amdgcn_exp2f(p0[r]);
; #pragma unroll
;     for (int r = 0; r < 16; ++r) p1[r] = __builtin_amdgcn_exp2f(p1[r]);
;     float ps = p0[0];
; #pragma unroll
;     for (int r = 1; r < 16; ++r) ps += p0[r];
; #pragma unroll
;     for (int r = 0; r < 16; ++r) ps += p1[r];
;     { auto rr = __builtin_amdgcn_permlane32_swap(__float_as_uint(ps), __float_as_uint(ps), false, false); ps = __uint_as_float(rr[0]) + __uint_as_float(rr[1]); }
;     l_reg += ps;
;     ...
;     PK4(p0, 0, pa0); PK4(p0, 8, pa1); PK4(p1, 0, pa2); PK4(p1, 8, pa3);
; template <int DQK, bool HASQK, bool HASPV>
; __device__ __forceinline__ void seg_m2(const int (&ka_)[4], int vb_, const bf16x8* qr, f32x16& p0, f32x16& p1, const float nm, f32x16 (&o)[4], bf16x8 pa0, bf16x8 pa1, bf16x8 pa2, bf16x8 pa3) {
;     ...
;     slot_read<DQK, HASQK, HASPV, 0>(kf, vf, ka_, vb_); slot_read<DQK, HASQK, HASPV, 1>(kf, vf, ka_, vb_); slot_read<DQK, HASQK, HASPV, 2>(kf, vf, ka_, vb_); slot_read<DQK, HASQK, HASPV, 3>(kf, vf, ka_, vb_);
;     SBAR();
;     f32x16 negm;
; #pragma unroll
;     for (int r = 0; r < 16; ++r) negm[r] = nm;
;     asm volatile("" : "+v"(negm));
;     SBAR();
.LBB0_605:
	v_exp_f32_e32 v96, v96
	v_exp_f32_e32 v97, v97
	v_exp_f32_e32 v98, v98
	v_exp_f32_e32 v99, v99
	v_exp_f32_e32 v100, v100
	v_exp_f32_e32 v101, v101
	v_add_f32_e32 v160, v96, v97
	v_exp_f32_e32 v102, v102
	v_add_f32_e32 v160, v98, v160
	v_exp_f32_e32 v103, v103
	v_add_f32_e32 v160, v99, v160
	v_exp_f32_e32 v104, v104
	v_add_f32_e32 v160, v100, v160
	v_exp_f32_e32 v105, v105
	v_add_f32_e32 v160, v101, v160
	v_exp_f32_e32 v106, v106
	v_add_f32_e32 v160, v102, v160
	v_exp_f32_e32 v107, v107
	v_add_f32_e32 v160, v103, v160
	v_exp_f32_e32 v108, v108
	v_add_f32_e32 v160, v104, v160
	v_exp_f32_e32 v109, v109
	v_add_f32_e32 v160, v105, v160
	v_exp_f32_e32 v110, v110
	v_add_f32_e32 v160, v106, v160
	v_exp_f32_e32 v111, v111
	v_add_f32_e32 v160, v107, v160
	v_exp_f32_e32 v80, v80
	v_add_f32_e32 v160, v108, v160
	v_exp_f32_e32 v81, v81
	v_add_f32_e32 v160, v109, v160
	v_exp_f32_e32 v82, v82
	v_add_f32_e32 v160, v110, v160
	v_exp_f32_e32 v83, v83
	v_add_f32_e32 v160, v111, v160
	v_exp_f32_e32 v84, v84
	v_add_f32_e32 v160, v80, v160
	v_exp_f32_e32 v85, v85
	v_add_f32_e32 v160, v81, v160
	v_exp_f32_e32 v86, v86
	v_add_f32_e32 v160, v82, v160
	v_exp_f32_e32 v87, v87
	v_add_f32_e32 v160, v83, v160
	v_exp_f32_e32 v88, v88
	v_add_f32_e32 v160, v84, v160
	v_exp_f32_e32 v89, v89
	v_add_f32_e32 v160, v85, v160
	v_exp_f32_e32 v90, v90
	v_add_f32_e32 v160, v86, v160
	v_exp_f32_e32 v91, v91
	v_add_f32_e32 v160, v87, v160
	v_exp_f32_e32 v92, v92
	v_add_f32_e32 v160, v88, v160
	v_exp_f32_e32 v93, v93
	v_add_f32_e32 v160, v89, v160
	v_exp_f32_e32 v94, v94
	v_add_f32_e32 v160, v90, v160
	v_exp_f32_e32 v95, v95
	v_add_f32_e32 v160, v91, v160
	v_add_f32_e32 v160, v92, v160
	v_add_f32_e32 v160, v93, v160
	v_add_f32_e32 v160, v94, v160
	v_add_f32_e32 v160, v95, v160
	v_mov_b32_e32 v161, v160
	s_nop 1
	v_permlane32_swap_b32_e32 v160, v161
	v_add_f32_e32 v160, v160, v161
	v_add_f32_e32 v204, v204, v160
	v_cvt_pk_bf16_f32 v172, v96, v97
	v_cvt_pk_bf16_f32 v173, v98, v99
	v_cvt_pk_bf16_f32 v174, v100, v101
	v_cvt_pk_bf16_f32 v175, v102, v103
	v_cvt_pk_bf16_f32 v168, v104, v105
	v_cvt_pk_bf16_f32 v169, v106, v107
	v_cvt_pk_bf16_f32 v170, v108, v109
	v_cvt_pk_bf16_f32 v171, v110, v111
	v_cvt_pk_bf16_f32 v164, v80, v81
	v_cvt_pk_bf16_f32 v165, v82, v83
	v_cvt_pk_bf16_f32 v166, v84, v85
	v_cvt_pk_bf16_f32 v167, v86, v87
	v_cvt_pk_bf16_f32 v160, v88, v89
	v_cvt_pk_bf16_f32 v161, v90, v91
	v_cvt_pk_bf16_f32 v162, v92, v93
	v_cvt_pk_bf16_f32 v163, v94, v95
	s_mul_i32 s47, s26, 0x6000
	s_addk_i32 s93, 0xc000
	s_cmp_lg_u32 s26, 0
	s_cselect_b32 s46, s93, 0x8000
	v_add_u32_e32 v227, s46, v202
	v_add_u32_e32 v207, s47, v185
	v_add_u32_e32 v224, s47, v187
	v_add_u32_e32 v225, s47, v205
	v_add_u32_e32 v226, s47, v206
	s_waitcnt lgkmcnt(0)
	ds_read_b64_tr_b16 v[208:209], v227 offset:0
	ds_read_b64_tr_b16 v[210:211], v227 offset:2048
	ds_read_b64_tr_b16 v[212:213], v227 offset:512
	ds_read_b64_tr_b16 v[214:215], v227 offset:2560
	ds_read_b64_tr_b16 v[216:217], v227 offset:1024
	ds_read_b64_tr_b16 v[218:219], v227 offset:3072
	ds_read_b64_tr_b16 v[220:221], v227 offset:1536
	ds_read_b64_tr_b16 v[222:223], v227 offset:3584
	v_xor_b32_e32 v80, 0x80000000, v203
	v_mov_b32_e32 v81, v80
	v_mov_b32_e32 v82, v80
	v_mov_b32_e32 v83, v80
	v_mov_b32_e32 v84, v80
	v_mov_b32_e32 v85, v80
	v_mov_b32_e32 v86, v80
	v_mov_b32_e32 v87, v80
	v_mov_b32_e32 v88, v80
	v_mov_b32_e32 v89, v80
	v_mov_b32_e32 v90, v80
	v_mov_b32_e32 v91, v80
	v_mov_b32_e32 v92, v80
	v_mov_b32_e32 v93, v80
	v_mov_b32_e32 v94, v80
	v_mov_b32_e32 v95, v80
	s_barrier
; template <int DQK, bool HASQK, bool HASPV, int J>
; __device__ __forceinline__ void slot_read(bf16x8 (&kf)[DQK / 16][2], s16x4 (&vf)[4][8], const int (&ka_)[4], int vb_) {
;     constexpr int NQS = HASQK ? 2 * (DQK / 16) : 0, NS = NQS + (HASPV ? 16 : 0);
;     if constexpr (J < NQS) { constexpr int d0 = J >> 1, h = J & 1; dsr128<(d0 >> 2) * 128 + h * 32 * DQK * 2>(kf[d0][h], ka_[d0 & 3]); }
;     else if constexpr (J < NS) { constexpr int q = J - NQS, g = q >> 2, d = q & 3; dstr64<v_rd_off(d, g, 0)>(vf[g][2 * d], vb_); dstr64<v_rd_off(d, g, 1)>(vf[g][2 * d + 1], vb_); }
; }
; template <int DQK, bool HASQK, bool HASPV, int J> ...
;     constexpr int NQS = HASQK ? 2 * (DQK / 16) : 0, NS = NQS + (HASPV ? 16 : 0);
;     if constexpr (J < NS) {
;         constexpr int rd1 = (J + 1 < NS) ? ((J + 1 < NQS) ? 1 : 2) : 0, rd2 = (J + 2 < NS) ? ((J + 2 < NQS) ? 1 : 2) : 0, rd3 = (J + 3 < NS) ? ((J + 3 < NQS) ? 1 : 2) : 0, NW = rd1 + rd2 + rd3;
;     ...
;         if constexpr (J < NQS) { constexpr int d0 = J >> 1, h = J & 1;
;             LWN1(kf[d0][h]); SBAR();
;             if constexpr (h == 0) p0 = __builtin_amdgcn_mfma_f32_32x32x16_bf16(kf[d0][0], qr[d0], (d0 == 0) ? negm : p0, 0, 0, 0);
;             else p1 = __builtin_amdgcn_mfma_f32_32x32x16_bf16(kf[d0][1], qr[d0], (d0 == 0) ? negm : p1, 0, 0, 0);
;         } else { constexpr int q = J - NQS, g = q >> 2, d = q & 3;
;             LWN2(vf[g][2 * d], vf[g][2 * d + 1]); SBAR();
;             o[d] = __builtin_amdgcn_mfma_f32_32x32x16_bf16(pa[g], (bf16x8){vf[g][2 * d][0], vf[g][2 * d][1], vf[g][2 * d][2], vf[g][2 * d][3], vf[g][2 * d + 1][0], vf[g][2 * d + 1][1], vf[g][2 * d + 1][2], vf[g][2 * d + 1][3]}, o[d], 0, 0, 0);
;         }
;     ...
;         SBAR();
;         slot_read<DQK, HASQK, HASPV, J + 4>(kf, vf, ka_, vb_);
;         SBAR();
;         slot_run<DQK, HASQK, HASPV, J + 1>(kf, vf, ka_, vb_, qr, p0, p1, negm, o, pa);
;     }
; }
;     ...
;     for (int i = 0; i < NT - 1; ++i) {
;         SEG_S(i);
;         { const int cp = (ci == 0) ? 2 : ci - 1, cn = (ci == 2) ? 0 : ci + 1;
;           if (DMA_M) { if (i + 3 < NT) DMA_K(i + 3, cp); if (i + 2 < NT) DMA_V(i + 2, cn); }
;           SEG_M(true, true, ci, cp);
;           if (DMA_M && i + 3 < NT) asm volatile("s_waitcnt vmcnt(%0)" :: "n"(NKW + 2) : "memory");
;           else asm volatile("s_waitcnt vmcnt(0)" ::: "memory");
;           BAR_ALL(); }
	s_waitcnt lgkmcnt(6)
	v_mfma_f32_32x32x16_bf16 v[64:79], v[172:175], v[208:211], v[64:79]
	ds_read_b64_tr_b16 v[208:209], v227 offset:4096
	ds_read_b64_tr_b16 v[210:211], v227 offset:6144
	s_waitcnt lgkmcnt(6)
	v_mfma_f32_32x32x16_bf16 v[48:63], v[172:175], v[212:215], v[48:63]
	ds_read_b64_tr_b16 v[212:213], v227 offset:4608
	ds_read_b64_tr_b16 v[214:215], v227 offset:6656
	s_waitcnt lgkmcnt(6)
	v_mfma_f32_32x32x16_bf16 v[32:47], v[172:175], v[216:219], v[32:47]
	ds_read_b64_tr_b16 v[216:217], v227 offset:5120
	ds_read_b64_tr_b16 v[218:219], v227 offset:7168
	s_waitcnt lgkmcnt(6)
	v_mfma_f32_32x32x16_bf16 v[16:31], v[172:175], v[220:223], v[16:31]
	ds_read_b64_tr_b16 v[220:221], v227 offset:5632
	ds_read_b64_tr_b16 v[222:223], v227 offset:7680
	s_waitcnt lgkmcnt(6)
	v_mfma_f32_32x32x16_bf16 v[64:79], v[168:171], v[208:211], v[64:79]
	ds_read_b64_tr_b16 v[208:209], v227 offset:8192
	ds_read_b64_tr_b16 v[210:211], v227 offset:10240
	s_waitcnt lgkmcnt(6)
	v_mfma_f32_32x32x16_bf16 v[48:63], v[168:171], v[212:215], v[48:63]
	ds_read_b64_tr_b16 v[212:213], v227 offset:8704
	ds_read_b64_tr_b16 v[214:215], v227 offset:10752
	s_waitcnt lgkmcnt(6)
	v_mfma_f32_32x32x16_bf16 v[32:47], v[168:171], v[216:219], v[32:47]
	ds_read_b64_tr_b16 v[216:217], v227 offset:9216
	ds_read_b64_tr_b16 v[218:219], v227 offset:11264
	s_waitcnt lgkmcnt(6)
	v_mfma_f32_32x32x16_bf16 v[16:31], v[168:171], v[220:223], v[16:31]
	ds_read_b64_tr_b16 v[220:221], v227 offset:9728
	ds_read_b64_tr_b16 v[222:223], v227 offset:11776
	s_waitcnt lgkmcnt(6)
	v_mfma_f32_32x32x16_bf16 v[64:79], v[164:167], v[208:211], v[64:79]
	ds_read_b64_tr_b16 v[208:209], v227 offset:12288
	ds_read_b64_tr_b16 v[210:211], v227 offset:14336
	s_waitcnt lgkmcnt(6)
	v_mfma_f32_32x32x16_bf16 v[48:63], v[164:167], v[212:215], v[48:63]
	ds_read_b64_tr_b16 v[212:213], v227 offset:12800
	ds_read_b64_tr_b16 v[214:215], v227 offset:14848
	s_waitcnt lgkmcnt(6)
	v_mfma_f32_32x32x16_bf16 v[32:47], v[164:167], v[216:219], v[32:47]
	ds_read_b64_tr_b16 v[216:217], v227 offset:13312
	ds_read_b64_tr_b16 v[218:219], v227 offset:15360
	s_waitcnt lgkmcnt(6)
	v_mfma_f32_32x32x16_bf16 v[16:31], v[164:167], v[220:223], v[16:31]
	ds_read_b64_tr_b16 v[220:221], v227 offset:13824
	ds_read_b64_tr_b16 v[222:223], v227 offset:15872
	s_waitcnt lgkmcnt(6)
	v_mfma_f32_32x32x16_bf16 v[64:79], v[160:163], v[208:211], v[64:79]
	ds_read_b128 v[208:211], v207 offset:0
	s_waitcnt lgkmcnt(5)
	v_mfma_f32_32x32x16_bf16 v[48:63], v[160:163], v[212:215], v[48:63]
	ds_read_b128 v[212:215], v207 offset:12288
	s_waitcnt lgkmcnt(4)
	v_mfma_f32_32x32x16_bf16 v[32:47], v[160:163], v[216:219], v[32:47]
	ds_read_b128 v[216:219], v224 offset:0
	s_waitcnt lgkmcnt(3)
	v_mfma_f32_32x32x16_bf16 v[16:31], v[160:163], v[220:223], v[16:31]
	ds_read_b128 v[220:223], v224 offset:12288
	s_waitcnt lgkmcnt(3)
	v_mfma_f32_32x32x16_bf16 v[96:111], v[208:211], v[112:115], v[80:95]
	ds_read_b128 v[208:211], v225 offset:0
	s_waitcnt lgkmcnt(3)
	v_mfma_f32_32x32x16_bf16 v[80:95], v[212:215], v[112:115], v[80:95]
	ds_read_b128 v[212:215], v225 offset:12288
	s_waitcnt lgkmcnt(3)
	v_mfma_f32_32x32x16_bf16 v[96:111], v[216:219], v[116:119], v[96:111]
	ds_read_b128 v[216:219], v226 offset:0
	s_waitcnt lgkmcnt(3)
	v_mfma_f32_32x32x16_bf16 v[80:95], v[220:223], v[116:119], v[80:95]
	ds_read_b128 v[220:223], v226 offset:12288
	s_waitcnt lgkmcnt(3)
	v_mfma_f32_32x32x16_bf16 v[96:111], v[208:211], v[120:123], v[96:111]
	ds_read_b128 v[208:211], v207 offset:128
	s_waitcnt lgkmcnt(3)
	v_mfma_f32_32x32x16_bf16 v[80:95], v[212:215], v[120:123], v[80:95]
	ds_read_b128 v[212:215], v207 offset:12416
	s_waitcnt lgkmcnt(3)
	v_mfma_f32_32x32x16_bf16 v[96:111], v[216:219], v[124:127], v[96:111]
	ds_read_b128 v[216:219], v224 offset:128
	s_waitcnt lgkmcnt(3)
	v_mfma_f32_32x32x16_bf16 v[80:95], v[220:223], v[124:127], v[80:95]
	ds_read_b128 v[220:223], v224 offset:12416
	s_waitcnt lgkmcnt(3)
	v_mfma_f32_32x32x16_bf16 v[96:111], v[208:211], v[128:131], v[96:111]
	ds_read_b128 v[208:211], v225 offset:128
	s_waitcnt lgkmcnt(3)
	v_mfma_f32_32x32x16_bf16 v[80:95], v[212:215], v[128:131], v[80:95]
	ds_read_b128 v[212:215], v225 offset:12416
	s_waitcnt lgkmcnt(3)
	v_mfma_f32_32x32x16_bf16 v[96:111], v[216:219], v[132:135], v[96:111]
	ds_read_b128 v[216:219], v226 offset:128
	s_waitcnt lgkmcnt(3)
	v_mfma_f32_32x32x16_bf16 v[80:95], v[220:223], v[132:135], v[80:95]
	ds_read_b128 v[220:223], v226 offset:12416
	s_waitcnt lgkmcnt(3)
	v_mfma_f32_32x32x16_bf16 v[96:111], v[208:211], v[136:139], v[96:111]
	ds_read_b128 v[208:211], v207 offset:256
	s_waitcnt lgkmcnt(3)
	v_mfma_f32_32x32x16_bf16 v[80:95], v[212:215], v[136:139], v[80:95]
	ds_read_b128 v[212:215], v207 offset:12544
	s_waitcnt lgkmcnt(3)
	v_mfma_f32_32x32x16_bf16 v[96:111], v[216:219], v[140:143], v[96:111]
	ds_read_b128 v[216:219], v224 offset:256
	s_waitcnt lgkmcnt(3)
	v_mfma_f32_32x32x16_bf16 v[80:95], v[220:223], v[140:143], v[80:95]
	ds_read_b128 v[220:223], v224 offset:12544
	s_waitcnt lgkmcnt(3)
	v_mfma_f32_32x32x16_bf16 v[96:111], v[208:211], v[144:147], v[96:111]
	ds_read_b128 v[208:211], v225 offset:256
	s_waitcnt lgkmcnt(3)
	v_mfma_f32_32x32x16_bf16 v[80:95], v[212:215], v[144:147], v[80:95]
	ds_read_b128 v[212:215], v225 offset:12544
	s_waitcnt lgkmcnt(3)
	v_mfma_f32_32x32x16_bf16 v[96:111], v[216:219], v[148:151], v[96:111]
	ds_read_b128 v[216:219], v226 offset:256
	s_waitcnt lgkmcnt(3)
	v_mfma_f32_32x32x16_bf16 v[80:95], v[220:223], v[148:151], v[80:95]
	ds_read_b128 v[220:223], v226 offset:12544
	s_waitcnt lgkmcnt(3)
	v_mfma_f32_32x32x16_bf16 v[96:111], v[208:211], v[152:155], v[96:111]
	s_waitcnt lgkmcnt(2)
	v_mfma_f32_32x32x16_bf16 v[80:95], v[212:215], v[152:155], v[80:95]
	s_waitcnt lgkmcnt(1)
	v_mfma_f32_32x32x16_bf16 v[96:111], v[216:219], v[156:159], v[96:111]
	s_waitcnt lgkmcnt(0)
	v_mfma_f32_32x32x16_bf16 v[80:95], v[220:223], v[156:159], v[80:95]
	s_waitcnt vmcnt(0)
	s_waitcnt lgkmcnt(0)
	s_barrier
	s_add_u32 s44, s44, 0x18000
	s_addc_u32 s45, s45, 0
	v_lshl_add_u64 v[194:195], v[194:195], 0, s[28:29]
	s_cmp_eq_u32 s44, 0xbe8000
	v_lshl_add_u64 v[196:197], v[196:197], 0, s[28:29]
	s_cbranch_scc1 .LBB0_616
